# combine phase: second token's expert-row gathers and residual loads issued at the top of the pair iteration (overlap with first token's work)
# baseline (speedup 1.0000x reference)
.LBB0_1089:
	s_waitcnt vmcnt(6)
	v_mov_b64_e32 v[80:81], v[96:97]
	s_add_i32 s2, s2, 2
	s_andn2_b64 vcc, exec, s[6:7]
	v_mov_b64_e32 v[82:83], v[98:99]
	s_mov_b32 s4, s20
	v_mov_b64_e32 v[86:87], v[90:91]
	v_mov_b64_e32 v[84:85], v[88:89]
	s_cbranch_vccz .LBB0_1110

.LBB0_1094:
	s_waitcnt vmcnt(2)
	v_ashrrev_i32_e32 v89, 31, v92
	v_mov_b32_e32 v88, v92
	v_lshlrev_b64 v[88:89], 10, v[88:89]
	v_lshl_add_u64 v[88:89], v[124:125], 0, v[88:89]
	global_load_dwordx4 v[96:99], v[88:89], off
	v_ashrrev_i32_e32 v89, 31, v93
	v_mov_b32_e32 v88, v93
	v_lshlrev_b64 v[88:89], 10, v[88:89]
	v_lshl_add_u64 v[88:89], v[124:125], 0, v[88:89]
	global_load_dwordx4 v[106:109], v[88:89], off
	v_ashrrev_i32_e32 v89, 31, v94
	v_mov_b32_e32 v88, v94
	v_lshlrev_b64 v[88:89], 10, v[88:89]
	s_add_i32 s20, s4, 1
	v_lshl_add_u64 v[88:89], v[124:125], 0, v[88:89]
	s_cmp_ge_i32 s20, s12
	global_load_dwordx4 v[110:113], v[88:89], off
	v_ashrrev_i32_e32 v89, 31, v95
	v_mov_b32_e32 v88, v95
	s_cselect_b64 s[6:7], -1, 0
	s_cmp_lt_i32 s20, s12
	v_lshlrev_b64 v[88:89], 10, v[88:89]
	s_cselect_b32 s3, s20, s4
	v_lshl_add_u64 v[88:89], v[124:125], 0, v[88:89]
	s_lshl_b32 s4, s3, 1
	global_load_dwordx4 v[114:117], v[88:89], off
	s_ashr_i32 s5, s4, 31
	s_lshl_b64 s[8:9], s[4:5], 4
	s_add_u32 s4, s13, s8
	s_addc_u32 s5, s14, s9
	s_add_u32 s8, s15, s8
	s_addc_u32 s9, s16, s9
	s_ashr_i32 s3, s2, 31
	s_lshl_b64 s[10:11], s[2:3], 11
	v_lshl_add_u64 v[88:89], v[122:123], 0, s[10:11]
	global_load_dwordx4 v[92:95], v[88:89], off
	s_nop 0
	global_load_dwordx4 v[88:91], v[88:89], off offset:16
	v_ashrrev_i32_e32 v185, 31, v84
	v_mov_b32_e32 v184, v84
	v_lshlrev_b64 v[184:185], 10, v[184:185]
	v_lshl_add_u64 v[184:185], v[124:125], 0, v[184:185]
	global_load_dwordx4 v[222:225], v[184:185], off
	v_ashrrev_i32_e32 v185, 31, v85
	v_mov_b32_e32 v184, v85
	v_lshlrev_b64 v[184:185], 10, v[184:185]
	v_lshl_add_u64 v[184:185], v[124:125], 0, v[184:185]
	global_load_dwordx4 v[226:229], v[184:185], off
	v_ashrrev_i32_e32 v185, 31, v86
	v_mov_b32_e32 v184, v86
	v_lshlrev_b64 v[184:185], 10, v[184:185]
	v_lshl_add_u64 v[184:185], v[124:125], 0, v[184:185]
	global_load_dwordx4 v[230:233], v[184:185], off
	v_ashrrev_i32_e32 v185, 31, v87
	v_mov_b32_e32 v184, v87
	v_lshlrev_b64 v[184:185], 10, v[184:185]
	v_lshl_add_u64 v[184:185], v[124:125], 0, v[184:185]
	global_load_dwordx4 v[244:247], v[184:185], off
	s_add_i32 s24, s2, 1
	s_ashr_i32 s25, s24, 31
	s_lshl_b64 s[24:25], s[24:25], 11
	v_lshl_add_u64 v[186:187], v[122:123], 0, s[24:25]
	global_load_dwordx4 v[192:195], v[186:187], off
	global_load_dwordx4 v[196:199], v[186:187], off offset:16
	s_waitcnt vmcnt(12)
	v_mov_b32_e32 v104, v103
	s_mov_b32 s22, 0x3d800000
	s_mov_b32 s10, 0x3fd744fd
	v_cndmask_b32_e64 v121, 0, 1, s[0:1]
	s_waitcnt vmcnt(11)
	v_cvt_pk_f32_fp8_sdwa v[136:137], v96 src0_sel:WORD_1
	v_cvt_pk_f32_fp8_e32 v[118:119], v96
	v_cvt_pk_f32_fp8_sdwa v[140:141], v97 src0_sel:WORD_1
	v_cvt_pk_f32_fp8_e32 v[138:139], v97
	v_cvt_pk_f32_fp8_e32 v[146:147], v98
	s_waitcnt vmcnt(10)
	v_cvt_pk_f32_fp8_sdwa v[144:145], v106 src0_sel:WORD_1
	v_cvt_pk_f32_fp8_e32 v[142:143], v106
	v_cvt_pk_f32_fp8_sdwa v[154:155], v107 src0_sel:WORD_1
	v_cvt_pk_f32_fp8_e32 v[152:153], v107
	v_pk_mul_f32 v[144:145], v[100:101], v[144:145] op_sel:[1,0]
	v_pk_mul_f32 v[142:143], v[100:101], v[142:143] op_sel:[1,0]
	v_pk_fma_f32 v[136:137], v[100:101], v[136:137], v[144:145] op_sel_hi:[0,1,1]
	s_waitcnt vmcnt(9)
	v_cvt_pk_f32_fp8_sdwa v[160:161], v110 src0_sel:WORD_1
	v_cvt_pk_f32_fp8_e32 v[150:151], v110
	v_cvt_pk_f32_fp8_e32 v[162:163], v111
	v_cvt_pk_f32_fp8_sdwa v[164:165], v111 src0_sel:WORD_1
	v_pk_fma_f32 v[118:119], v[100:101], v[118:119], v[142:143] op_sel_hi:[0,1,1]
	v_cvt_pk_f32_fp8_e32 v[156:157], v108
	v_cvt_pk_f32_fp8_sdwa v[158:159], v108 src0_sel:WORD_1
	v_cvt_pk_f32_fp8_sdwa v[148:149], v98 src0_sel:WORD_1
	v_cvt_pk_f32_fp8_e32 v[166:167], v112
	s_waitcnt vmcnt(8)
	v_cvt_pk_f32_fp8_sdwa v[172:173], v114 src0_sel:WORD_1
	v_cvt_pk_f32_fp8_e32 v[170:171], v114
	v_cvt_pk_f32_fp8_e32 v[174:175], v115
	v_cvt_pk_f32_fp8_sdwa v[114:115], v115 src0_sel:WORD_1
	v_pk_mul_f32 v[172:173], v[104:105], v[172:173] op_sel_hi:[0,1]
	v_pk_fma_f32 v[144:145], v[102:103], v[160:161], v[172:173] op_sel_hi:[0,1,1]
	v_pk_add_f32 v[136:137], v[136:137], v[144:145]
	v_pk_mul_f32 v[144:145], v[34:35], s[22:23] op_sel_hi:[1,0]
	v_pk_mul_f32 v[170:171], v[104:105], v[170:171] op_sel_hi:[0,1]
	s_waitcnt vmcnt(7)
	v_lshlrev_b32_e32 v160, 16, v92
	v_and_b32_e32 v161, 0xffff0000, v92
	v_lshlrev_b32_e32 v92, 16, v93
	v_and_b32_e32 v93, 0xffff0000, v93
	v_pk_mul_f32 v[136:137], v[144:145], v[136:137]
	v_pk_fma_f32 v[142:143], v[102:103], v[150:151], v[170:171] op_sel_hi:[0,1,1]
	v_pk_fma_f32 v[136:137], v[92:93], s[10:11], v[136:137] op_sel_hi:[1,0,1]
	v_pk_mul_f32 v[92:93], v[100:101], v[154:155] op_sel:[1,0]
	v_pk_add_f32 v[118:119], v[118:119], v[142:143]
	v_pk_mul_f32 v[142:143], v[100:101], v[152:153] op_sel:[1,0]
	v_pk_fma_f32 v[92:93], v[100:101], v[140:141], v[92:93] op_sel_hi:[0,1,1]
	v_pk_mul_f32 v[114:115], v[104:105], v[114:115] op_sel_hi:[0,1]
	v_pk_mul_f32 v[140:141], v[104:105], v[174:175] op_sel_hi:[0,1]
	v_cvt_pk_f32_fp8_e32 v[176:177], v116
	v_cvt_pk_f32_fp8_sdwa v[178:179], v116 src0_sel:WORD_1
	v_pk_fma_f32 v[138:139], v[100:101], v[138:139], v[142:143] op_sel_hi:[0,1,1]
	v_pk_fma_f32 v[140:141], v[102:103], v[162:163], v[140:141] op_sel_hi:[0,1,1]
	v_pk_fma_f32 v[114:115], v[102:103], v[164:165], v[114:115] op_sel_hi:[0,1,1]
	v_cvt_pk_f32_fp8_sdwa v[168:169], v112 src0_sel:WORD_1
	v_pk_add_f32 v[92:93], v[92:93], v[114:115]
	v_pk_add_f32 v[114:115], v[138:139], v[140:141]
	v_pk_mul_f32 v[138:139], v[38:39], s[22:23] op_sel_hi:[1,0]
	v_lshlrev_b32_e32 v170, 16, v94
	v_and_b32_e32 v171, 0xffff0000, v94
	v_lshlrev_b32_e32 v94, 16, v95
	v_and_b32_e32 v95, 0xffff0000, v95
	v_pk_mul_f32 v[92:93], v[138:139], v[92:93]
	v_cvt_pk_f32_fp8_e32 v[106:107], v109
	v_pk_fma_f32 v[154:155], v[94:95], s[10:11], v[92:93] op_sel_hi:[1,0,1]
	v_pk_mul_f32 v[94:95], v[100:101], v[156:157] op_sel:[1,0]
	v_cvt_pk_f32_fp8_sdwa v[108:109], v109 src0_sel:WORD_1
	v_cvt_pk_f32_fp8_e32 v[180:181], v117
	v_cvt_pk_f32_fp8_sdwa v[116:117], v117 src0_sel:WORD_1
	v_pk_mul_f32 v[92:93], v[100:101], v[158:159] op_sel:[1,0]
	v_pk_fma_f32 v[94:95], v[100:101], v[146:147], v[94:95] op_sel_hi:[0,1,1]
	v_pk_mul_f32 v[140:141], v[104:105], v[178:179] op_sel_hi:[0,1]
	v_pk_mul_f32 v[146:147], v[104:105], v[176:177] op_sel_hi:[0,1]
	v_cvt_pk_f32_fp8_e32 v[96:97], v99
	v_cvt_pk_f32_fp8_sdwa v[98:99], v99 src0_sel:WORD_1
	v_cvt_pk_f32_fp8_e32 v[110:111], v113
	v_cvt_pk_f32_fp8_sdwa v[112:113], v113 src0_sel:WORD_1
	v_pk_fma_f32 v[92:93], v[100:101], v[148:149], v[92:93] op_sel_hi:[0,1,1]
	v_pk_fma_f32 v[146:147], v[102:103], v[166:167], v[146:147] op_sel_hi:[0,1,1]
	v_pk_fma_f32 v[140:141], v[102:103], v[168:169], v[140:141] op_sel_hi:[0,1,1]
	v_pk_add_f32 v[92:93], v[92:93], v[140:141]
	v_pk_add_f32 v[94:95], v[94:95], v[146:147]
	v_pk_mul_f32 v[140:141], v[42:43], s[22:23] op_sel_hi:[1,0]
	v_pk_mul_f32 v[148:149], v[40:41], s[22:23] op_sel_hi:[1,0]
	s_waitcnt vmcnt(6)
	v_lshlrev_b32_e32 v172, 16, v88
	v_and_b32_e32 v173, 0xffff0000, v88
	v_lshlrev_b32_e32 v88, 16, v89
	v_and_b32_e32 v89, 0xffff0000, v89
	v_pk_mul_f32 v[94:95], v[148:149], v[94:95]
	v_pk_mul_f32 v[92:93], v[140:141], v[92:93]
	v_pk_fma_f32 v[158:159], v[172:173], s[10:11], v[94:95] op_sel_hi:[1,0,1]
	v_pk_fma_f32 v[156:157], v[88:89], s[10:11], v[92:93] op_sel_hi:[1,0,1]
	v_pk_mul_f32 v[88:89], v[100:101], v[108:109] op_sel:[1,0]
	v_pk_mul_f32 v[94:95], v[104:105], v[116:117] op_sel_hi:[0,1]
	v_pk_mul_f32 v[150:151], v[32:33], s[22:23] op_sel_hi:[1,0]
	v_pk_fma_f32 v[88:89], v[100:101], v[98:99], v[88:89] op_sel_hi:[0,1,1]
	v_pk_fma_f32 v[94:95], v[102:103], v[112:113], v[94:95] op_sel_hi:[0,1,1]
	v_pk_mul_f32 v[118:119], v[150:151], v[118:119]
	v_pk_mul_f32 v[142:143], v[36:37], s[22:23] op_sel_hi:[1,0]
	v_pk_add_f32 v[88:89], v[88:89], v[94:95]
	v_pk_mul_f32 v[146:147], v[50:51], s[22:23] op_sel_hi:[1,0]
	v_lshlrev_b32_e32 v182, 16, v90
	v_and_b32_e32 v183, 0xffff0000, v90
	v_lshlrev_b32_e32 v90, 16, v91
	v_and_b32_e32 v91, 0xffff0000, v91
	v_pk_fma_f32 v[118:119], v[160:161], s[10:11], v[118:119] op_sel_hi:[1,0,1]
	v_pk_mul_f32 v[114:115], v[142:143], v[114:115]
	v_pk_mul_f32 v[92:93], v[100:101], v[106:107] op_sel:[1,0]
	v_pk_mul_f32 v[88:89], v[146:147], v[88:89]
	v_pk_fma_f32 v[114:115], v[170:171], s[10:11], v[114:115] op_sel_hi:[1,0,1]
	v_pk_fma_f32 v[92:93], v[100:101], v[96:97], v[92:93] op_sel_hi:[0,1,1]
	v_pk_mul_f32 v[96:97], v[104:105], v[180:181] op_sel_hi:[0,1]
	v_pk_fma_f32 v[116:117], v[90:91], s[10:11], v[88:89] op_sel_hi:[1,0,1]
	v_add_f32_e32 v88, v118, v119
	v_add_f32_e32 v89, v136, v137
	v_pk_fma_f32 v[96:97], v[102:103], v[110:111], v[96:97] op_sel_hi:[0,1,1]
	v_add_f32_e32 v88, v88, v89
	v_add_f32_e32 v89, v114, v115
	v_add_f32_e32 v90, v154, v155
	v_pk_add_f32 v[92:93], v[92:93], v[96:97]
	v_pk_mul_f32 v[152:153], v[48:49], s[22:23] op_sel_hi:[1,0]
	v_add_f32_e32 v88, 0, v88
	v_add_f32_e32 v89, v89, v90
	v_pk_mul_f32 v[92:93], v[152:153], v[92:93]
	v_add_f32_e32 v88, v88, v89
	v_add_f32_e32 v89, v158, v159
	v_add_f32_e32 v90, v156, v157
	v_pk_fma_f32 v[160:161], v[182:183], s[10:11], v[92:93] op_sel_hi:[1,0,1]
	v_add_f32_e32 v89, v89, v90
	v_add_f32_e32 v88, v88, v89
	v_add_f32_e32 v89, v160, v161
	v_add_f32_e32 v90, v116, v117
	v_add_f32_e32 v89, v89, v90
	v_add_f32_e32 v88, v88, v89
	ds_swizzle_b32 v89, v88 offset:swizzle(SWAP,1)
	s_mov_b64 s[10:11], -1
	s_waitcnt lgkmcnt(0)
	v_add_f32_e32 v88, v88, v89
	ds_swizzle_b32 v89, v88 offset:swizzle(SWAP,2)
	s_waitcnt lgkmcnt(0)
	v_add_f32_e32 v88, v88, v89
	ds_swizzle_b32 v89, v88 offset:swizzle(SWAP,4)
	s_waitcnt lgkmcnt(0)
	v_add_f32_e32 v88, v88, v89
	ds_swizzle_b32 v89, v88 offset:swizzle(SWAP,8)
	s_waitcnt lgkmcnt(0)
	v_add_f32_e32 v104, v88, v89
	global_load_dwordx4 v[88:91], v201, s[4:5] offset:16
	global_load_dwordx4 v[92:95], v201, s[4:5]
	global_load_dwordx4 v[96:99], v201, s[8:9] offset:16
	global_load_dwordx4 v[100:103], v201, s[8:9]
	ds_swizzle_b32 v105, v104 offset:swizzle(SWAP,16)
	s_mov_b32 s4, 0x3727c5ac
	s_lshl_b64 s[8:9], s[2:3], 10
	s_waitcnt lgkmcnt(0)
	v_add_f32_e32 v104, v104, v105
	v_mov_b32_e32 v105, v104
	s_nop 1
	v_permlane32_swap_b32_e32 v104, v105
	v_add_f32_e32 v104, v104, v105
	v_fmac_f32_e32 v137, 0xba800000, v104
	v_fmac_f32_e32 v119, 0xba800000, v104
	v_fmamk_f32 v136, v104, 0xba800000, v136
	v_fmamk_f32 v118, v104, 0xba800000, v118
	v_mul_f32_e32 v105, v119, v119
	v_mul_f32_e32 v106, v137, v137
	v_fmac_f32_e32 v105, v118, v118
	v_fmac_f32_e32 v106, v136, v136
	v_fmac_f32_e32 v155, 0xba800000, v104
	v_fmac_f32_e32 v115, 0xba800000, v104
	v_add_f32_e32 v105, v105, v106
	v_fmamk_f32 v154, v104, 0xba800000, v154
	v_fmamk_f32 v114, v104, 0xba800000, v114
	v_mul_f32_e32 v106, v115, v115
	v_mul_f32_e32 v107, v155, v155
	v_fmac_f32_e32 v106, v114, v114
	v_fmac_f32_e32 v107, v154, v154
	v_add_f32_e32 v106, v106, v107
	v_fmac_f32_e32 v157, 0xba800000, v104
	v_fmac_f32_e32 v159, 0xba800000, v104
	v_add_f32_e32 v105, v105, v106
	v_fmamk_f32 v156, v104, 0xba800000, v156
	v_fmamk_f32 v158, v104, 0xba800000, v158
	v_mul_f32_e32 v106, v159, v159
	v_mul_f32_e32 v107, v157, v157
	v_fmac_f32_e32 v106, v158, v158
	v_fmac_f32_e32 v107, v156, v156
	v_add_f32_e32 v106, v106, v107
	v_fmac_f32_e32 v117, 0xba800000, v104
	v_fmac_f32_e32 v161, 0xba800000, v104
	v_add_f32_e32 v105, v106, v105
	v_fmamk_f32 v116, v104, 0xba800000, v116
	v_fmamk_f32 v160, v104, 0xba800000, v160
	v_mul_f32_e32 v104, v161, v161
	v_mul_f32_e32 v106, v117, v117
	v_fmac_f32_e32 v104, v160, v160
	v_fmac_f32_e32 v106, v116, v116
	v_add_f32_e32 v104, v104, v106
	v_add_f32_e32 v104, v104, v105
	ds_swizzle_b32 v105, v104 offset:swizzle(SWAP,1)
	s_waitcnt lgkmcnt(0)
	v_add_f32_e32 v104, v104, v105
	ds_swizzle_b32 v105, v104 offset:swizzle(SWAP,2)
	s_waitcnt lgkmcnt(0)
	v_add_f32_e32 v104, v104, v105
	ds_swizzle_b32 v105, v104 offset:swizzle(SWAP,4)
	s_waitcnt lgkmcnt(0)
	v_add_f32_e32 v104, v104, v105
	ds_swizzle_b32 v105, v104 offset:swizzle(SWAP,8)
	s_waitcnt lgkmcnt(0)
	v_add_f32_e32 v104, v104, v105
	ds_swizzle_b32 v105, v104 offset:swizzle(SWAP,16)
	s_waitcnt lgkmcnt(0)
	v_add_f32_e32 v104, v104, v105
	v_mov_b32_e32 v105, v104
	s_nop 1
	v_permlane32_swap_b32_e32 v104, v105
	v_add_f32_e32 v104, v104, v105
	v_mov_b32_e32 v105, s4
	v_fmac_f32_e32 v105, 0x3a800000, v104
	s_mov_b32 s4, 0x800000
	v_mul_f32_e32 v104, 0x4b800000, v105
	v_cmp_gt_f32_e32 vcc, s4, v105
	v_readlane_b32 s4, v254, 28
	v_readlane_b32 s5, v254, 29
	v_cndmask_b32_e32 v104, v105, v104, vcc
	v_rsq_f32_e32 v104, v104
	s_nop 0
	v_mul_f32_e32 v105, 0x45800000, v104
	v_cndmask_b32_e32 v162, v104, v105, vcc
	v_pk_mul_f32 v[104:105], v[118:119], v[162:163] op_sel_hi:[1,0]
	v_pk_mul_f32 v[106:107], v[136:137], v[162:163] op_sel_hi:[1,0]
	v_pk_mul_f32 v[108:109], v[114:115], v[162:163] op_sel_hi:[1,0]
	v_pk_mul_f32 v[110:111], v[154:155], v[162:163] op_sel_hi:[1,0]
	v_pk_mul_f32 v[112:113], v[158:159], v[162:163] op_sel_hi:[1,0]
	v_pk_mul_f32 v[114:115], v[156:157], v[162:163] op_sel_hi:[1,0]
	v_pk_mul_f32 v[136:137], v[160:161], v[162:163] op_sel_hi:[1,0]
	v_pk_mul_f32 v[116:117], v[116:117], v[162:163] op_sel_hi:[1,0]
	v_pk_fma_f32 v[106:107], v[14:15], v[106:107], v[30:31]
	v_pk_fma_f32 v[104:105], v[12:13], v[104:105], v[28:29]
	v_pk_fma_f32 v[110:111], v[10:11], v[110:111], v[26:27]
	v_pk_fma_f32 v[108:109], v[8:9], v[108:109], v[24:25]
	v_pk_fma_f32 v[114:115], v[6:7], v[114:115], v[22:23]
	v_pk_fma_f32 v[112:113], v[4:5], v[112:113], v[20:21]
	v_pk_fma_f32 v[118:119], v[2:3], v[116:117], v[18:19]
	v_pk_fma_f32 v[116:117], v[0:1], v[136:137], v[16:17]
	s_and_b64 vcc, exec, s[4:5]
	v_pk_add_f32 v[136:137], v[44:45], 1.0 op_sel_hi:[1,0]
	v_cmp_ne_u32_e64 s[4:5], 1, v121
	s_cbranch_vccz .LBB0_1100
	v_cvt_pk_bf16_f32 v154, v104, v105
	v_cvt_pk_bf16_f32 v155, v106, v107
	v_lshl_add_u64 v[158:159], s[8:9], 1, v[130:131]
	v_cvt_pk_bf16_f32 v156, v108, v109
	v_cvt_pk_bf16_f32 v157, v110, v111
	global_store_dwordx4 v[158:159], v[154:157], off
	v_pk_add_f32 v[160:161], v[60:61], 1.0 op_sel_hi:[1,0]
	v_pk_add_f32 v[164:165], v[56:57], 1.0 op_sel_hi:[1,0]
	v_cvt_pk_bf16_f32 v154, v112, v113
	v_cvt_pk_bf16_f32 v155, v114, v115
	v_cvt_pk_bf16_f32 v156, v116, v117
	v_cvt_pk_bf16_f32 v157, v118, v119
	global_store_dwordx4 v[158:159], v[154:157], off offset:16
	v_pk_add_f32 v[158:159], v[62:63], 1.0 op_sel_hi:[1,0]
	v_pk_fma_f32 v[162:163], v[160:161], v[108:109], v[68:69]
	v_pk_add_f32 v[154:155], v[46:47], 1.0 op_sel_hi:[1,0]
	v_pk_add_f32 v[160:161], v[58:59], 1.0 op_sel_hi:[1,0]
	v_pk_add_f32 v[168:169], v[52:53], 1.0 op_sel_hi:[1,0]
	v_pk_add_f32 v[166:167], v[54:55], 1.0 op_sel_hi:[1,0]
	v_pk_fma_f32 v[154:155], v[154:155], v[106:107], v[66:67]
	v_pk_fma_f32 v[156:157], v[136:137], v[104:105], v[64:65]
	v_pk_fma_f32 v[158:159], v[158:159], v[110:111], v[70:71]
	v_pk_fma_f32 v[160:161], v[160:161], v[114:115], v[74:75]
	v_pk_fma_f32 v[164:165], v[164:165], v[112:113], v[72:73]
	v_pk_fma_f32 v[166:167], v[166:167], v[118:119], v[78:79]
	v_pk_fma_f32 v[168:169], v[168:169], v[116:117], v[76:77]
	s_and_b64 vcc, exec, s[4:5]
	s_cbranch_vccnz .LBB0_1097
	v_mov_b32_e32 v170, v201
	v_mov_b32_e32 v171, v201
	v_mov_b32_e32 v172, v201
	v_mov_b32_e32 v173, v201
	v_cvt_pk_fp8_f32 v170, v156, v157
	v_cvt_pk_fp8_f32 v171, v162, v163
	v_cvt_pk_fp8_f32 v172, v164, v165
	v_cvt_pk_fp8_f32 v173, v168, v169
	v_cvt_pk_fp8_f32 v170, v154, v155 op_sel:[0,0,1]
	v_cvt_pk_fp8_f32 v171, v158, v159 op_sel:[0,0,1]
	v_cvt_pk_fp8_f32 v172, v160, v161 op_sel:[0,0,1]
	v_cvt_pk_fp8_f32 v173, v166, v167 op_sel:[0,0,1]
	v_lshl_add_u64 v[174:175], v[132:133], 0, s[8:9]
	s_mov_b64 s[10:11], 0
	global_store_dwordx4 v[174:175], v[170:173], off

.LBB0_1102:
	v_ashrrev_i32_e32 v105, 31, v84
	v_mov_b32_e32 v104, v84
	v_ashrrev_i32_e32 v109, 31, v85
	v_mov_b32_e32 v108, v85
	v_lshlrev_b64 v[104:105], 10, v[104:105]
	v_lshlrev_b64 v[84:85], 10, v[108:109]
	v_lshl_add_u64 v[104:105], v[124:125], 0, v[104:105]
	v_lshl_add_u64 v[84:85], v[124:125], 0, v[84:85]
	s_add_i32 s8, s2, 1
	v_ashrrev_i32_e32 v85, 31, v86
	v_mov_b32_e32 v84, v86
	v_lshlrev_b64 v[84:85], 10, v[84:85]
	v_lshl_add_u64 v[84:85], v[124:125], 0, v[84:85]
	v_ashrrev_i32_e32 v85, 31, v87
	v_mov_b32_e32 v84, v87
	v_lshlrev_b64 v[84:85], 10, v[84:85]
	v_lshl_add_u64 v[84:85], v[124:125], 0, v[84:85]
	s_ashr_i32 s9, s8, 31
	s_lshl_b64 s[10:11], s[8:9], 11
	v_lshl_add_u64 v[84:85], v[122:123], 0, s[10:11]
	v_mov_b32_e32 v84, v83
	s_mov_b32 s10, 0x3fd744fd
	s_mov_b32 s3, 0x3727c5ac
	v_readlane_b32 s22, v254, 28
	v_readlane_b32 s23, v254, 29
	s_lshl_b64 s[8:9], s[8:9], 10
	s_waitcnt vmcnt(9)
	v_mov_b64_e32 v[104:105], v[222:223]
	v_mov_b64_e32 v[106:107], v[224:225]
	v_mov_b64_e32 v[108:109], v[226:227]
	v_mov_b64_e32 v[110:111], v[228:229]
	v_mov_b64_e32 v[154:155], v[230:231]
	v_mov_b64_e32 v[156:157], v[232:233]
	v_mov_b64_e32 v[174:175], v[244:245]
	v_mov_b64_e32 v[176:177], v[246:247]
	v_cvt_pk_f32_fp8_e32 v[202:203], v104
	v_cvt_pk_f32_fp8_sdwa v[204:205], v104 src0_sel:WORD_1
	v_cvt_pk_f32_fp8_e32 v[190:191], v105
	v_cvt_pk_f32_fp8_sdwa v[168:169], v105 src0_sel:WORD_1
	v_cvt_pk_f32_fp8_e32 v[114:115], v106
	v_cvt_pk_f32_fp8_sdwa v[116:117], v106 src0_sel:WORD_1
	v_cvt_pk_f32_fp8_e32 v[86:87], v107
	v_cvt_pk_f32_fp8_sdwa v[104:105], v107 src0_sel:WORD_1
	v_cvt_pk_f32_fp8_e32 v[206:207], v108
	v_cvt_pk_f32_fp8_sdwa v[208:209], v108 src0_sel:WORD_1
	v_cvt_pk_f32_fp8_e32 v[210:211], v109
	v_cvt_pk_f32_fp8_sdwa v[212:213], v109 src0_sel:WORD_1
	v_cvt_pk_f32_fp8_e32 v[160:161], v110
	v_cvt_pk_f32_fp8_sdwa v[162:163], v110 src0_sel:WORD_1
	v_cvt_pk_f32_fp8_e32 v[106:107], v111
	v_cvt_pk_f32_fp8_sdwa v[108:109], v111 src0_sel:WORD_1
	v_cvt_pk_f32_fp8_e32 v[218:219], v174
	v_cvt_pk_f32_fp8_sdwa v[220:221], v174 src0_sel:WORD_1
	v_cvt_pk_f32_fp8_e32 v[214:215], v154
	v_cvt_pk_f32_fp8_sdwa v[216:217], v154 src0_sel:WORD_1
	v_cvt_pk_f32_fp8_e32 v[178:179], v155
	v_cvt_pk_f32_fp8_sdwa v[180:181], v155 src0_sel:WORD_1
	v_cvt_pk_f32_fp8_e32 v[164:165], v156
	v_cvt_pk_f32_fp8_sdwa v[166:167], v156 src0_sel:WORD_1
	v_cvt_pk_f32_fp8_e32 v[110:111], v157
	v_cvt_pk_f32_fp8_sdwa v[112:113], v157 src0_sel:WORD_1
	v_cvt_pk_f32_fp8_e32 v[184:185], v175
	v_cvt_pk_f32_fp8_sdwa v[188:189], v175 src0_sel:WORD_1
	v_cvt_pk_f32_fp8_e32 v[172:173], v176
	v_cvt_pk_f32_fp8_sdwa v[174:175], v176 src0_sel:WORD_1
	v_cvt_pk_f32_fp8_e32 v[154:155], v177
	v_cvt_pk_f32_fp8_sdwa v[156:157], v177 src0_sel:WORD_1
	s_waitcnt vmcnt(8)
	v_lshlrev_b32_e32 v182, 16, v194
	v_and_b32_e32 v183, 0xffff0000, v194
	v_lshlrev_b32_e32 v186, 16, v195
	v_and_b32_e32 v187, 0xffff0000, v195
	s_waitcnt vmcnt(7)
	v_lshlrev_b32_e32 v170, 16, v196
	v_and_b32_e32 v171, 0xffff0000, v196
	v_lshlrev_b32_e32 v176, 16, v197
	v_and_b32_e32 v177, 0xffff0000, v197
	v_lshlrev_b32_e32 v118, 16, v198
	v_and_b32_e32 v119, 0xffff0000, v198
	v_lshlrev_b32_e32 v158, 16, v199
	v_and_b32_e32 v159, 0xffff0000, v199
	v_pk_mul_f32 v[194:195], v[80:81], v[208:209] op_sel:[1,0]
	v_pk_mul_f32 v[196:197], v[80:81], v[206:207] op_sel:[1,0]
	v_pk_mul_f32 v[198:199], v[84:85], v[220:221] op_sel_hi:[0,1]
	v_pk_mul_f32 v[206:207], v[84:85], v[218:219] op_sel_hi:[0,1]
	v_pk_mul_f32 v[208:209], v[80:81], v[212:213] op_sel:[1,0]
	v_pk_mul_f32 v[210:211], v[80:81], v[210:211] op_sel:[1,0]
	v_pk_mul_f32 v[162:163], v[80:81], v[162:163] op_sel:[1,0]
	v_pk_mul_f32 v[160:161], v[80:81], v[160:161] op_sel:[1,0]
	v_pk_mul_f32 v[108:109], v[80:81], v[108:109] op_sel:[1,0]
	v_pk_mul_f32 v[106:107], v[80:81], v[106:107] op_sel:[1,0]
	v_pk_fma_f32 v[196:197], v[80:81], v[202:203], v[196:197] op_sel_hi:[0,1,1]
	v_pk_fma_f32 v[194:195], v[80:81], v[204:205], v[194:195] op_sel_hi:[0,1,1]
	v_pk_fma_f32 v[202:203], v[82:83], v[214:215], v[206:207] op_sel_hi:[0,1,1]
	v_pk_fma_f32 v[198:199], v[82:83], v[216:217], v[198:199] op_sel_hi:[0,1,1]
	v_pk_fma_f32 v[190:191], v[80:81], v[190:191], v[210:211] op_sel_hi:[0,1,1]
	v_pk_fma_f32 v[168:169], v[80:81], v[168:169], v[208:209] op_sel_hi:[0,1,1]
	v_pk_mul_f32 v[188:189], v[84:85], v[188:189] op_sel_hi:[0,1]
	v_pk_mul_f32 v[184:185], v[84:85], v[184:185] op_sel_hi:[0,1]
	v_pk_fma_f32 v[114:115], v[80:81], v[114:115], v[160:161] op_sel_hi:[0,1,1]
	v_pk_fma_f32 v[116:117], v[80:81], v[116:117], v[162:163] op_sel_hi:[0,1,1]
	v_pk_mul_f32 v[160:161], v[84:85], v[174:175] op_sel_hi:[0,1]
	v_pk_mul_f32 v[162:163], v[84:85], v[172:173] op_sel_hi:[0,1]
	v_pk_fma_f32 v[86:87], v[80:81], v[86:87], v[106:107] op_sel_hi:[0,1,1]
	v_pk_fma_f32 v[80:81], v[80:81], v[104:105], v[108:109] op_sel_hi:[0,1,1]
	v_pk_mul_f32 v[104:105], v[84:85], v[156:157] op_sel_hi:[0,1]
	v_pk_mul_f32 v[84:85], v[84:85], v[154:155] op_sel_hi:[0,1]
	v_pk_add_f32 v[194:195], v[194:195], v[198:199]
	v_pk_add_f32 v[196:197], v[196:197], v[202:203]
	v_pk_fma_f32 v[178:179], v[82:83], v[178:179], v[184:185] op_sel_hi:[0,1,1]
	v_pk_fma_f32 v[180:181], v[82:83], v[180:181], v[188:189] op_sel_hi:[0,1,1]
	v_pk_fma_f32 v[162:163], v[82:83], v[164:165], v[162:163] op_sel_hi:[0,1,1]
	v_pk_fma_f32 v[160:161], v[82:83], v[166:167], v[160:161] op_sel_hi:[0,1,1]
	v_pk_fma_f32 v[84:85], v[82:83], v[110:111], v[84:85] op_sel_hi:[0,1,1]
	v_pk_fma_f32 v[82:83], v[82:83], v[112:113], v[104:105] op_sel_hi:[0,1,1]
	v_lshlrev_b32_e32 v222, 16, v192
	v_and_b32_e32 v223, 0xffff0000, v192
	v_lshlrev_b32_e32 v192, 16, v193
	v_and_b32_e32 v193, 0xffff0000, v193
	v_pk_mul_f32 v[150:151], v[150:151], v[196:197]
	v_pk_mul_f32 v[144:145], v[144:145], v[194:195]
	v_pk_add_f32 v[168:169], v[168:169], v[180:181]
	v_pk_add_f32 v[178:179], v[190:191], v[178:179]
	v_pk_add_f32 v[80:81], v[80:81], v[82:83]
	v_pk_fma_f32 v[144:145], v[192:193], s[10:11], v[144:145] op_sel_hi:[1,0,1]
	v_pk_fma_f32 v[150:151], v[222:223], s[10:11], v[150:151] op_sel_hi:[1,0,1]
	v_pk_mul_f32 v[142:143], v[142:143], v[178:179]
	v_pk_mul_f32 v[138:139], v[138:139], v[168:169]
	v_pk_add_f32 v[82:83], v[86:87], v[84:85]
	v_pk_mul_f32 v[80:81], v[146:147], v[80:81]
	v_pk_fma_f32 v[138:139], v[186:187], s[10:11], v[138:139] op_sel_hi:[1,0,1]
	v_pk_fma_f32 v[142:143], v[182:183], s[10:11], v[142:143] op_sel_hi:[1,0,1]
	v_pk_add_f32 v[116:117], v[116:117], v[160:161]
	v_pk_add_f32 v[114:115], v[114:115], v[162:163]
	v_pk_mul_f32 v[82:83], v[152:153], v[82:83]
	v_pk_fma_f32 v[108:109], v[158:159], s[10:11], v[80:81] op_sel_hi:[1,0,1]
	v_add_f32_e32 v80, v150, v151
	v_add_f32_e32 v81, v144, v145
	v_pk_mul_f32 v[114:115], v[148:149], v[114:115]
	v_pk_mul_f32 v[116:117], v[140:141], v[116:117]
	v_pk_fma_f32 v[110:111], v[118:119], s[10:11], v[82:83] op_sel_hi:[1,0,1]
	v_add_f32_e32 v80, v80, v81
	v_add_f32_e32 v81, v142, v143
	v_add_f32_e32 v82, v138, v139
	v_pk_fma_f32 v[116:117], v[176:177], s[10:11], v[116:117] op_sel_hi:[1,0,1]
	v_pk_fma_f32 v[114:115], v[170:171], s[10:11], v[114:115] op_sel_hi:[1,0,1]
	v_add_f32_e32 v80, 0, v80
	v_add_f32_e32 v81, v81, v82
	v_add_f32_e32 v80, v80, v81
	v_add_f32_e32 v81, v114, v115
	v_add_f32_e32 v82, v116, v117
	v_add_f32_e32 v81, v81, v82
	v_add_f32_e32 v80, v80, v81
	v_add_f32_e32 v81, v110, v111
	v_add_f32_e32 v82, v108, v109
	v_add_f32_e32 v81, v81, v82
	v_add_f32_e32 v80, v80, v81
	ds_swizzle_b32 v81, v80 offset:swizzle(SWAP,1)
	s_mov_b64 s[10:11], -1
	s_waitcnt lgkmcnt(0)
	v_add_f32_e32 v80, v80, v81
	ds_swizzle_b32 v81, v80 offset:swizzle(SWAP,2)
	s_waitcnt lgkmcnt(0)
	v_add_f32_e32 v80, v80, v81
	ds_swizzle_b32 v81, v80 offset:swizzle(SWAP,4)
	s_waitcnt lgkmcnt(0)
	v_add_f32_e32 v80, v80, v81
	ds_swizzle_b32 v81, v80 offset:swizzle(SWAP,8)
	s_waitcnt lgkmcnt(0)
	v_add_f32_e32 v80, v80, v81
	ds_swizzle_b32 v81, v80 offset:swizzle(SWAP,16)
	s_waitcnt lgkmcnt(0)
	v_add_f32_e32 v80, v80, v81
	v_mov_b32_e32 v81, v80
	s_nop 1
	v_permlane32_swap_b32_e32 v80, v81
	v_add_f32_e32 v80, v80, v81
	v_fmac_f32_e32 v145, 0xba800000, v80
	v_fmac_f32_e32 v151, 0xba800000, v80
	v_fmamk_f32 v144, v80, 0xba800000, v144
	v_fmamk_f32 v150, v80, 0xba800000, v150
	v_mul_f32_e32 v81, v151, v151
	v_mul_f32_e32 v82, v145, v145
	v_fmac_f32_e32 v81, v150, v150
	v_fmac_f32_e32 v82, v144, v144
	v_fmac_f32_e32 v139, 0xba800000, v80
	v_fmac_f32_e32 v143, 0xba800000, v80
	v_add_f32_e32 v81, v81, v82
	v_fmamk_f32 v138, v80, 0xba800000, v138
	v_fmamk_f32 v142, v80, 0xba800000, v142
	v_mul_f32_e32 v82, v143, v143
	v_mul_f32_e32 v83, v139, v139
	v_fmac_f32_e32 v82, v142, v142
	v_fmac_f32_e32 v83, v138, v138
	v_add_f32_e32 v82, v82, v83
	v_fmac_f32_e32 v117, 0xba800000, v80
	v_fmac_f32_e32 v115, 0xba800000, v80
	v_add_f32_e32 v81, v81, v82
	v_fmamk_f32 v116, v80, 0xba800000, v116
	v_fmamk_f32 v114, v80, 0xba800000, v114
	v_mul_f32_e32 v82, v115, v115
	v_mul_f32_e32 v83, v117, v117
	v_fmac_f32_e32 v82, v114, v114
	v_fmac_f32_e32 v83, v116, v116
	v_add_f32_e32 v82, v82, v83
	v_fmac_f32_e32 v109, 0xba800000, v80
	v_fmac_f32_e32 v111, 0xba800000, v80
	v_add_f32_e32 v81, v82, v81
	v_fmamk_f32 v108, v80, 0xba800000, v108
	v_fmamk_f32 v110, v80, 0xba800000, v110
	v_mul_f32_e32 v80, v111, v111
	v_mul_f32_e32 v82, v109, v109
	v_fmac_f32_e32 v80, v110, v110
	v_fmac_f32_e32 v82, v108, v108
	v_add_f32_e32 v80, v80, v82
	v_add_f32_e32 v80, v80, v81
	ds_swizzle_b32 v81, v80 offset:swizzle(SWAP,1)
	s_waitcnt lgkmcnt(0)
	v_add_f32_e32 v80, v80, v81
	ds_swizzle_b32 v81, v80 offset:swizzle(SWAP,2)
	s_waitcnt lgkmcnt(0)
	v_add_f32_e32 v80, v80, v81
	ds_swizzle_b32 v81, v80 offset:swizzle(SWAP,4)
	s_waitcnt lgkmcnt(0)
	v_add_f32_e32 v80, v80, v81
	ds_swizzle_b32 v81, v80 offset:swizzle(SWAP,8)
	s_waitcnt lgkmcnt(0)
	v_add_f32_e32 v80, v80, v81
	ds_swizzle_b32 v81, v80 offset:swizzle(SWAP,16)
	s_waitcnt lgkmcnt(0)
	v_add_f32_e32 v80, v80, v81
	v_mov_b32_e32 v81, v80
	s_nop 1
	v_permlane32_swap_b32_e32 v80, v81
	v_add_f32_e32 v80, v80, v81
	v_mov_b32_e32 v81, s3
	v_fmac_f32_e32 v81, 0x3a800000, v80
	s_mov_b32 s3, 0x800000
	v_mul_f32_e32 v80, 0x4b800000, v81
	v_cmp_gt_f32_e32 vcc, s3, v81
	s_nop 1
	v_cndmask_b32_e32 v80, v81, v80, vcc
	v_rsq_f32_e32 v80, v80
	s_nop 0
	v_mul_f32_e32 v81, 0x45800000, v80
	v_cndmask_b32_e32 v112, v80, v81, vcc
	v_pk_mul_f32 v[80:81], v[150:151], v[112:113] op_sel_hi:[1,0]
	v_pk_mul_f32 v[82:83], v[144:145], v[112:113] op_sel_hi:[1,0]
	v_pk_mul_f32 v[84:85], v[142:143], v[112:113] op_sel_hi:[1,0]
	v_pk_mul_f32 v[86:87], v[138:139], v[112:113] op_sel_hi:[1,0]
	v_pk_mul_f32 v[104:105], v[114:115], v[112:113] op_sel_hi:[1,0]
	v_pk_mul_f32 v[106:107], v[116:117], v[112:113] op_sel_hi:[1,0]
	v_pk_mul_f32 v[114:115], v[110:111], v[112:113] op_sel_hi:[1,0]
	v_pk_mul_f32 v[108:109], v[108:109], v[112:113] op_sel_hi:[1,0]
	v_pk_fma_f32 v[82:83], v[14:15], v[82:83], v[30:31]
	v_pk_fma_f32 v[80:81], v[12:13], v[80:81], v[28:29]
	v_pk_fma_f32 v[86:87], v[10:11], v[86:87], v[26:27]
	v_pk_fma_f32 v[84:85], v[8:9], v[84:85], v[24:25]
	v_pk_fma_f32 v[106:107], v[6:7], v[106:107], v[22:23]
	v_pk_fma_f32 v[104:105], v[4:5], v[104:105], v[20:21]
	v_pk_fma_f32 v[110:111], v[2:3], v[108:109], v[18:19]
	v_pk_fma_f32 v[108:109], v[0:1], v[114:115], v[16:17]
	s_and_b64 vcc, exec, s[22:23]
	s_cbranch_vccz .LBB0_1108
	v_cvt_pk_bf16_f32 v112, v80, v81
	v_cvt_pk_bf16_f32 v113, v82, v83
	v_cvt_pk_bf16_f32 v114, v84, v85
	v_cvt_pk_bf16_f32 v115, v86, v87
	v_lshl_add_u64 v[116:117], s[8:9], 1, v[130:131]
	global_store_dwordx4 v[116:117], v[112:115], off
	v_pk_add_f32 v[118:119], v[60:61], 1.0 op_sel_hi:[1,0]
	v_pk_add_f32 v[138:139], v[56:57], 1.0 op_sel_hi:[1,0]
	v_cvt_pk_bf16_f32 v112, v104, v105
	v_cvt_pk_bf16_f32 v113, v106, v107
	v_cvt_pk_bf16_f32 v114, v108, v109
	v_cvt_pk_bf16_f32 v115, v110, v111
	global_store_dwordx4 v[116:117], v[112:115], off offset:16
	v_pk_add_f32 v[116:117], v[62:63], 1.0 op_sel_hi:[1,0]
	v_pk_add_f32 v[142:143], v[52:53], 1.0 op_sel_hi:[1,0]
	v_pk_add_f32 v[112:113], v[46:47], 1.0 op_sel_hi:[1,0]
	v_pk_fma_f32 v[114:115], v[136:137], v[80:81], v[64:65]
	v_pk_fma_f32 v[136:137], v[118:119], v[84:85], v[68:69]
	v_pk_add_f32 v[118:119], v[58:59], 1.0 op_sel_hi:[1,0]
	v_pk_add_f32 v[140:141], v[54:55], 1.0 op_sel_hi:[1,0]
	v_pk_fma_f32 v[112:113], v[112:113], v[82:83], v[66:67]
	v_pk_fma_f32 v[116:117], v[116:117], v[86:87], v[70:71]
	v_pk_fma_f32 v[118:119], v[118:119], v[106:107], v[74:75]
	v_pk_fma_f32 v[138:139], v[138:139], v[104:105], v[72:73]
	v_pk_fma_f32 v[140:141], v[140:141], v[110:111], v[78:79]
	v_pk_fma_f32 v[142:143], v[142:143], v[108:109], v[76:77]
	s_and_b64 vcc, exec, s[4:5]
	s_mov_b64 s[4:5], -1
	s_cbranch_vccnz .LBB0_1105
	v_mov_b32_e32 v144, v201
	v_mov_b32_e32 v145, v201
	v_mov_b32_e32 v146, v201
	v_mov_b32_e32 v147, v201
	v_cvt_pk_fp8_f32 v144, v114, v115
	v_cvt_pk_fp8_f32 v145, v136, v137
	v_cvt_pk_fp8_f32 v146, v138, v139
	v_cvt_pk_fp8_f32 v147, v142, v143
	v_cvt_pk_fp8_f32 v144, v112, v113 op_sel:[0,0,1]
	v_cvt_pk_fp8_f32 v145, v116, v117 op_sel:[0,0,1]
	v_cvt_pk_fp8_f32 v146, v118, v119 op_sel:[0,0,1]
	v_cvt_pk_fp8_f32 v147, v140, v141 op_sel:[0,0,1]
	v_lshl_add_u64 v[148:149], v[132:133], 0, s[8:9]
	s_mov_b64 s[4:5], 0
	global_store_dwordx4 v[148:149], v[144:147], off
